# P3 queue: attention items popped from eight per-batch queue heads, a workgroup starts on its own XCC's head (K/V of a head stay in one L2), head order rotated per XCC, moves to the next head when empt
# speedup vs baseline: 1.0012x; 1.0012x over previous
.LBB0_407:
	s_add_u32 s0, s36, s6
	s_addc_u32 s1, s37, s7
	global_load_dwordx4 v[4:7], v1, s[0:1]
	global_load_dwordx4 v[8:11], v1, s[0:1] offset:16
	s_add_u32 s0, s38, s6
	s_addc_u32 s1, s39, s7
	global_load_dwordx4 v[12:15], v1, s[0:1]
	global_load_dwordx4 v[16:19], v1, s[0:1] offset:16
	s_add_u32 s0, s40, s6
	s_addc_u32 s1, s41, s7
	global_load_dwordx4 v[20:23], v1, s[0:1]
	global_load_dwordx4 v[24:27], v1, s[0:1] offset:16
	s_add_u32 s0, s42, s6
	s_addc_u32 s1, s43, s7
	global_load_dwordx4 v[28:31], v1, s[0:1]
	global_load_dwordx4 v[32:35], v1, s[0:1] offset:16
	s_add_u32 s6, s6, 32
	s_addc_u32 s7, s7, 0
	s_cmpk_eq_i32 s6, 0x100
	s_waitcnt vmcnt(7)
	v_mov_b32_e32 v36, v4
	v_mov_b32_e32 v4, v6
	s_waitcnt vmcnt(6)
	v_mov_b32_e32 v6, v8
	v_mov_b32_e32 v8, v10
	s_waitcnt vmcnt(5)
	v_mov_b32_e32 v10, v12
	v_mov_b32_e32 v12, v14
	s_waitcnt vmcnt(3)
	v_mov_b32_e32 v37, v20
	v_mov_b32_e32 v20, v5
	v_mov_b32_e32 v5, v22
	v_mov_b32_e32 v22, v7
	s_waitcnt vmcnt(2)
	v_mov_b32_e32 v7, v24
	v_mov_b32_e32 v24, v9
	v_mov_b32_e32 v9, v26
	v_mov_b32_e32 v26, v11
	s_waitcnt vmcnt(1)
	v_mov_b32_e32 v11, v28
	v_mov_b32_e32 v28, v13
	v_pk_fma_f32 v[2:3], v[36:37], v[10:11], v[2:3]
	v_mov_b32_e32 v13, v30
	v_pk_fma_f32 v[2:3], v[20:21], v[28:29], v[2:3]
	v_mov_b32_e32 v30, v15
	v_pk_fma_f32 v[2:3], v[4:5], v[12:13], v[2:3]
	v_mov_b32_e32 v14, v16
	s_waitcnt vmcnt(0)
	v_mov_b32_e32 v15, v32
	v_pk_fma_f32 v[2:3], v[22:23], v[30:31], v[2:3]
	v_mov_b32_e32 v32, v17
	v_pk_fma_f32 v[2:3], v[6:7], v[14:15], v[2:3]
	v_mov_b32_e32 v16, v18
	v_mov_b32_e32 v17, v34
	v_pk_fma_f32 v[2:3], v[24:25], v[32:33], v[2:3]
	v_mov_b32_e32 v34, v19
	v_pk_fma_f32 v[2:3], v[8:9], v[16:17], v[2:3]
	s_nop 0
	v_pk_fma_f32 v[2:3], v[26:27], v[34:35], v[2:3]
	s_cbranch_scc0 .LBB0_407
	v_mul_f32_e32 v1, 0x3fb8aa3b, v2
	v_mul_f32_e32 v2, 0x3fb8aa3b, v3
	v_exp_f32_e32 v1, v1
	v_exp_f32_e32 v2, v2
	s_add_u32 s0, s22, 0x4000000
	s_addc_u32 s1, s23, 0
	v_writelane_b32 v255, s0, 17
	v_sub_f32_e32 v1, v1, v2
	s_add_u32 s64, s20, 0x8000000
	v_add_f32_e32 v198, 0x3e4ccccd, v1
	v_writelane_b32 v255, s1, 18
	s_addc_u32 s65, s21, 0
	s_add_i32 s55, 0, 0x19000
	s_add_i32 s0, 0, 0x18c10
	s_mov_b32 s42, -2.0
	s_mov_b32 s48, 0xc1000000
	s_mov_b32 s50, 0xc1200000
	s_mov_b32 s56, 0xc1800000
	s_mov_b32 s58, 0xc1900000
	s_mov_b32 s60, 0xc1c00000
	s_mov_b32 s62, 0xc1d00000
	s_mov_b32 s68, 0xc2200000
	s_mov_b32 s70, 0xc2280000
	s_mov_b32 s72, 0xc2400000
	s_mov_b32 s74, 0xc2480000
	s_mov_b32 s76, 0xc2600000
	s_mov_b32 s78, 0xc2680000
	v_mov_b32_e32 v199, v198
	s_mov_b32 s41, 0
	s_mov_b64 s[6:7], -1
	v_mov_b32_e32 v3, 0
	s_movk_i32 s33, 0x2000
	s_movk_i32 s52, 0x4000
	s_movk_i32 s53, 0x6000
	s_mov_b32 s37, 0x8000
	s_mov_b32 s66, 0xa000
	s_mov_b32 s67, 0xc000
	s_mov_b32 s83, 0xe000
	s_mov_b32 s90, 0x10000
	s_mov_b32 s91, 0x12000
	s_mov_b32 s92, 0x14000
	s_mov_b32 s93, 0x16000
	s_movk_i32 s80, 0x1000
	s_movk_i32 s81, 0x3000
	s_movk_i32 s28, 0x5000
	s_mov_b32 s29, 0x40000
	s_mov_b32 s30, 0x41000
	v_writelane_b32 v255, s0, 19
	v_mov_b32_e32 v1, 0x260
	v_mov_b32_e32 v201, 2.0
	s_mov_b32 s43, 0xc0400000
	s_mov_b32 s49, 0xc1100000
	s_mov_b32 s51, 0xc1300000
	s_mov_b32 s57, 0xc1880000
	s_mov_b32 s59, 0xc1980000
	s_mov_b32 s61, 0xc1c80000
	s_mov_b32 s63, 0xc1d80000
	s_mov_b32 s69, 0xc2240000
	s_mov_b32 s71, 0xc22c0000
	s_mov_b32 s73, 0xc2440000
	s_mov_b32 s75, 0xc24c0000
	s_mov_b32 s77, 0xc2640000
	s_mov_b32 s79, 0xc26c0000
	s_mov_b32 s36, 0x41000000
	s_movk_i32 s4, 0x7fff
	v_mov_b32_e32 v213, s55
	v_mov_b32_e32 v214, 0x42800000
	v_mbcnt_hi_u32_b32 v212, -1, v196
	v_mov_b32_e32 v215, 0xf149f2ca
	s_mov_b64 s[84:85], -1
	s_mov_b32 s5, 0
	s_mov_b32 s32, 0
	s_getreg_b32 s98, hwreg(HW_REG_XCC_ID, 0, 4)
	s_and_b32 s98, s98, 7
	s_mov_b32 s99, 0
	s_branch .LBB0_412

.Lmy_pop_atomic:
	v_readlane_b32 s34, v255, 15
	v_readlane_b32 s35, v255, 16
	s_lshl_b32 s0, s98, 2
	s_add_i32 s0, s0, 64
	s_cmp_eq_u32 s31, 1
	s_cselect_b32 s0, s0, 48
	s_add_u32 s0, s34, s0
	s_addc_u32 s1, s35, 0
	v_mov_b32_e32 v4, 1
	global_atomic_add v4, v3, v4, s[0:1] sc0
.Lmy_pop_check:
	s_cmp_eq_u32 s31, 1
	s_cbranch_scc0 .LBB0_415
	s_waitcnt vmcnt(0)
	v_readfirstlane_b32 s0, v4
	s_nop 1
	s_cmpk_lt_u32 s0, 0x80
	s_cbranch_scc1 .Lmy_pop_ok
	s_cmp_eq_u32 s99, 7
	s_cbranch_scc1 .Lmy_pop_none
	s_add_i32 s99, s99, 1
	s_add_i32 s98, s98, 1
	s_and_b32 s98, s98, 7
	s_branch .Lmy_pop_atomic
.Lmy_pop_none:
	v_mov_b32_e32 v4, 0x400
	s_branch .LBB0_415
.Lmy_pop_ok:
	s_lshl_b32 s1, s98, 4
	s_add_i32 s0, s0, s1
	s_and_b32 s0, s0, 0x7f
	s_lshl_b32 s1, s98, 7
	s_or_b32 s0, s0, s1
	v_mov_b32_e32 v4, s0

.LBB0_553:
	s_lshl_b32 s31, s98, 2
	s_add_i32 s31, s31, 64
	s_bitcmp1_b32 s5, 0
	s_cselect_b64 s[6:7], -1, 0
	s_orn2_b64 s[6:7], s[6:7], s[84:85]
	s_cmp_lg_u64 s[6:7], 0
	s_cselect_b32 s31, s31, 48
	s_cselect_b32 s32, 1, 2
	v_readlane_b32 s6, v255, 15
	v_readlane_b32 s7, v255, 16
	v_mov_b32_e32 v253, 1
	v_cmp_eq_u32_e64 s[8:9], 0, v0
	s_add_u32 s6, s6, s31
	s_addc_u32 s7, s7, 0
	s_and_saveexec_b64 s[34:35], s[8:9]
	s_cbranch_execz .Lmy_pf_skip
	global_atomic_add v254, v3, v253, s[6:7] sc0

	.amdhsa_kernel _ZN12_GLOBAL__N_16k_megaENS_6ParamsE
		.amdhsa_group_segment_fixed_size 0
		.amdhsa_private_segment_fixed_size 0
		.amdhsa_kernarg_size 720
		.amdhsa_user_sgpr_count 2
		.amdhsa_user_sgpr_dispatch_ptr 0
		.amdhsa_user_sgpr_queue_ptr 0
		.amdhsa_user_sgpr_kernarg_segment_ptr 1
		.amdhsa_user_sgpr_dispatch_id 0
		.amdhsa_user_sgpr_kernarg_preload_length 0
		.amdhsa_user_sgpr_kernarg_preload_offset 0
		.amdhsa_user_sgpr_private_segment_size 0
		.amdhsa_uses_dynamic_stack 0
		.amdhsa_enable_private_segment 0
		.amdhsa_system_sgpr_workgroup_id_x 1
		.amdhsa_system_sgpr_workgroup_id_y 0
		.amdhsa_system_sgpr_workgroup_id_z 0
		.amdhsa_system_sgpr_workgroup_info 0
		.amdhsa_system_vgpr_workitem_id 0
		.amdhsa_next_free_vgpr 256
		.amdhsa_next_free_sgpr 100
		.amdhsa_accum_offset 256
		.amdhsa_reserve_vcc 1
		.amdhsa_float_round_mode_32 0
		.amdhsa_float_round_mode_16_64 0
		.amdhsa_float_denorm_mode_32 3
		.amdhsa_float_denorm_mode_16_64 3
		.amdhsa_dx10_clamp 1
		.amdhsa_ieee_mode 1
		.amdhsa_fp16_overflow 0
		.amdhsa_tg_split 0
		.amdhsa_exception_fp_ieee_invalid_op 0
		.amdhsa_exception_fp_denorm_src 0
		.amdhsa_exception_fp_ieee_div_zero 0
		.amdhsa_exception_fp_ieee_overflow 0
		.amdhsa_exception_fp_ieee_underflow 0
		.amdhsa_exception_fp_ieee_inexact 0
		.amdhsa_exception_int_div_zero 0
	.end_amdhsa_kernel

amdhsa.kernels:
  - .agpr_count:     0
    .args:
      - .offset:         0
        .size:           464
        .value_kind:     by_value
      - .offset:         464
        .size:           4
        .value_kind:     hidden_block_count_x
      - .offset:         468
        .size:           4
        .value_kind:     hidden_block_count_y
      - .offset:         472
        .size:           4
        .value_kind:     hidden_block_count_z
      - .offset:         476
        .size:           2
        .value_kind:     hidden_group_size_x
      - .offset:         478
        .size:           2
        .value_kind:     hidden_group_size_y
      - .offset:         480
        .size:           2
        .value_kind:     hidden_group_size_z
      - .offset:         482
        .size:           2
        .value_kind:     hidden_remainder_x
      - .offset:         484
        .size:           2
        .value_kind:     hidden_remainder_y
      - .offset:         486
        .size:           2
        .value_kind:     hidden_remainder_z
      - .offset:         504
        .size:           8
        .value_kind:     hidden_global_offset_x
      - .offset:         512
        .size:           8
        .value_kind:     hidden_global_offset_y
      - .offset:         520
        .size:           8
        .value_kind:     hidden_global_offset_z
      - .offset:         528
        .size:           2
        .value_kind:     hidden_grid_dims
      - .offset:         584
        .size:           4
        .value_kind:     hidden_dynamic_lds_size
    .group_segment_fixed_size: 0
    .kernarg_segment_align: 8
    .kernarg_segment_size: 720
    .language:       OpenCL C
    .language_version:
      - 2
      - 0
    .max_flat_workgroup_size: 512
    .name:           _ZN12_GLOBAL__N_16k_megaENS_6ParamsE
    .private_segment_fixed_size: 0
    .sgpr_count:     106
    .sgpr_spill_count: 20
    .symbol:         _ZN12_GLOBAL__N_16k_megaENS_6ParamsE.kd
    .uniform_work_group_size: 1
    .uses_dynamic_stack: false
    .vgpr_count:     256
    .vgpr_spill_count: 0
    .wavefront_size: 64
